# adds: MoE-up GEMM K-loop peeled as well (all five GEMM bodies start with SrcC=0 instead of zeroed accumulators)
# speedup vs baseline: 1.0115x; 1.0031x over previous
.LBB0_1246:
	s_lshl_b32 s0, s76, 2
	s_add_i32 s0, s0, 0
	v_mov_b32_e32 v173, v34
	v_mov_b32_e32 v175, v34
	s_add_i32 s0, s0, 0x23000
	s_mov_b32 s1, -2
	s_mov_b64 s[18:19], 0x100
	v_mov_b32_e32 v186, v168
	v_mov_b32_e32 v187, v170
	v_mov_b32_e32 v188, v172
	v_mov_b32_e32 v189, v174
	s_branch .Lpm_1248

.Lpm_1247:
	s_and_b64 s[46:47], s[42:43], exec
	s_cselect_b32 s47, 0, s18
	s_cselect_b32 s46, 0, s19
	s_add_u32 s48, s28, s47
	s_addc_u32 s49, s29, s46
	s_add_u32 s79, s2, s18
	s_addc_u32 s80, s3, s19
	s_add_u32 s46, s48, 0x80
	s_addc_u32 s47, s49, 0
	s_add_i32 s82, 0, 0x10000
	v_add_u32_e32 v6, s82, v184
	ds_read_b128 v[10:13], v6
	ds_read_b128 v[14:17], v6 offset:1024
	ds_read_b128 v[2:5], v6 offset:2048
	ds_read_b128 v[6:9], v6 offset:3072
	v_cndmask_b32_e64 v191, v168, v186, s[42:43]
	v_cndmask_b32_e64 v190, v170, v187, s[42:43]
	v_cndmask_b32_e64 v210, v172, v188, s[42:43]
	v_cndmask_b32_e64 v211, v174, v189, s[42:43]
	s_and_b64 s[42:43], s[42:43], exec
	s_cselect_b32 s43, s45, s80
	s_cselect_b32 s42, s44, s79
	s_add_u32 s79, s28, s18
	s_addc_u32 s81, s29, s19
	s_add_u32 s80, s79, 0xffffff80
	s_addc_u32 s81, s81, -1
	ds_read_b128 v[192:195], v185
	ds_read_b128 v[196:199], v185 offset:1024
	ds_read_b128 v[200:203], v185 offset:2048
	ds_read_b128 v[204:207], v185 offset:3072
	ds_read_b128 v[218:221], v185 offset:4096
	ds_read_b128 v[222:225], v185 offset:5120
	ds_read_b128 v[226:229], v185 offset:6144
	ds_read_b128 v[230:233], v185 offset:7168
	s_add_i32 m0, s59, 0xc000
	v_lshl_add_u64 v[18:19], s[80:81], 0, v[172:173]
	global_load_lds_dwordx4 v[18:19], off
	v_lshl_add_u64 v[18:19], s[80:81], 0, v[174:175]
	s_add_i32 m0, s59, 0xe000
	s_nop 0
	global_load_lds_dwordx4 v[18:19], off
	s_waitcnt lgkmcnt(8)
	s_barrier
	s_waitcnt lgkmcnt(0)
	s_setprio 1
	s_waitcnt lgkmcnt(0)
	v_mfma_scale_f32_16x16x128_f8f6f4 v[160:163], v[10:17], v[192:199], 0, v176, v35 op_sel_hi:[0,0,0]
	v_mfma_scale_f32_16x16x128_f8f6f4 v[152:155], v[2:9], v[192:199], 0, v176, v35 op_sel_hi:[0,0,0]
	v_mfma_scale_f32_16x16x128_f8f6f4 v[144:147], v[10:17], v[200:207], 0, v176, v35 op_sel_hi:[0,0,0]
	v_mfma_scale_f32_16x16x128_f8f6f4 v[136:139], v[2:9], v[200:207], 0, v176, v35 op_sel_hi:[0,0,0]
	v_mfma_scale_f32_16x16x128_f8f6f4 v[128:131], v[10:17], v[218:225], 0, v176, v35 op_sel_hi:[0,0,0]
	v_mfma_scale_f32_16x16x128_f8f6f4 v[120:123], v[2:9], v[218:225], 0, v176, v35 op_sel_hi:[0,0,0]
	v_mfma_scale_f32_16x16x128_f8f6f4 v[112:115], v[10:17], v[226:233], 0, v176, v35 op_sel_hi:[0,0,0]
	v_mfma_scale_f32_16x16x128_f8f6f4 v[104:107], v[2:9], v[226:233], 0, v176, v35 op_sel_hi:[0,0,0]
	s_setprio 0
	s_barrier
	s_add_i32 s79, 0, 0x14000
	v_add_u32_e32 v22, s79, v184
	s_mov_b64 s[80:81], s[42:43]
	s_add_i32 s82, s82, s58
	ds_read_b128 v[26:29], v22
	ds_read_b128 v[30:33], v22 offset:1024
	ds_read_b128 v[18:21], v22 offset:2048
	ds_read_b128 v[22:25], v22 offset:3072
	s_mov_b32 m0, s82
	v_lshl_add_u64 v[208:209], s[80:81], 0, v[164:165]
	global_load_lds_dwordx4 v[208:209], off
	v_lshl_add_u64 v[208:209], s[80:81], 0, v[166:167]
	s_add_i32 m0, s82, 0x2000
	s_nop 0
	global_load_lds_dwordx4 v[208:209], off
	s_barrier
	s_waitcnt lgkmcnt(0)
	s_setprio 1
	s_waitcnt lgkmcnt(0)
	v_mfma_scale_f32_16x16x128_f8f6f4 v[156:159], v[26:33], v[192:199], 0, v1, v35 op_sel_hi:[0,0,0]
	v_mfma_scale_f32_16x16x128_f8f6f4 v[148:151], v[18:25], v[192:199], 0, v1, v35 op_sel_hi:[0,0,0]
	v_mfma_scale_f32_16x16x128_f8f6f4 v[140:143], v[26:33], v[200:207], 0, v1, v35 op_sel_hi:[0,0,0]
	v_mfma_scale_f32_16x16x128_f8f6f4 v[132:135], v[18:25], v[200:207], 0, v1, v35 op_sel_hi:[0,0,0]
	v_mfma_scale_f32_16x16x128_f8f6f4 v[124:127], v[26:33], v[218:225], 0, v1, v35 op_sel_hi:[0,0,0]
	v_mfma_scale_f32_16x16x128_f8f6f4 v[116:119], v[18:25], v[218:225], 0, v1, v35 op_sel_hi:[0,0,0]
	v_mfma_scale_f32_16x16x128_f8f6f4 v[108:111], v[26:33], v[226:233], 0, v1, v35 op_sel_hi:[0,0,0]
	v_mfma_scale_f32_16x16x128_f8f6f4 v[100:103], v[18:25], v[226:233], 0, v1, v35 op_sel_hi:[0,0,0]
	s_setprio 0
	s_mov_b64 s[80:81], s[48:49]
	s_mov_b32 m0, s59
	s_barrier
	ds_read_b128 v[192:195], v185 offset:16384
	ds_read_b128 v[196:199], v185 offset:17408
	ds_read_b128 v[200:203], v185 offset:18432
	ds_read_b128 v[204:207], v185 offset:19456
	ds_read_b128 v[218:221], v185 offset:20480
	ds_read_b128 v[222:225], v185 offset:21504
	ds_read_b128 v[226:229], v185 offset:22528
	ds_read_b128 v[230:233], v185 offset:23552
	s_nop 0
	global_load_lds_dwordx4 v191, s[80:81]
	s_mov_b32 m0, s62
	s_nop 0
	global_load_lds_dwordx4 v190, s[80:81]
	s_barrier
	s_waitcnt lgkmcnt(0)
	s_setprio 1
	s_waitcnt lgkmcnt(0)
	v_mfma_scale_f32_16x16x128_f8f6f4 v[96:99], v[10:17], v[192:199], 0, v176, v35 op_sel_hi:[0,0,0]
	v_mfma_scale_f32_16x16x128_f8f6f4 v[88:91], v[2:9], v[192:199], 0, v176, v35 op_sel_hi:[0,0,0]
	v_mfma_scale_f32_16x16x128_f8f6f4 v[80:83], v[10:17], v[200:207], 0, v176, v35 op_sel_hi:[0,0,0]
	v_mfma_scale_f32_16x16x128_f8f6f4 v[72:75], v[2:9], v[200:207], 0, v176, v35 op_sel_hi:[0,0,0]
	v_mfma_scale_f32_16x16x128_f8f6f4 v[64:67], v[10:17], v[218:225], 0, v176, v35 op_sel_hi:[0,0,0]
	v_mfma_scale_f32_16x16x128_f8f6f4 v[56:59], v[2:9], v[218:225], 0, v176, v35 op_sel_hi:[0,0,0]
	v_mfma_scale_f32_16x16x128_f8f6f4 v[48:51], v[10:17], v[226:233], 0, v176, v35 op_sel_hi:[0,0,0]
	v_mfma_scale_f32_16x16x128_f8f6f4 v[40:43], v[2:9], v[226:233], 0, v176, v35 op_sel_hi:[0,0,0]
	s_setprio 0
	s_barrier
	s_add_u32 s80, s42, 0x20000
	s_addc_u32 s81, s43, 0
	s_add_i32 s79, s79, s58
	s_mov_b32 m0, s79
	v_lshl_add_u64 v[2:3], s[80:81], 0, v[164:165]
	global_load_lds_dwordx4 v[2:3], off
	v_lshl_add_u64 v[2:3], s[80:81], 0, v[166:167]
	s_add_i32 m0, s79, 0x2000
	s_nop 0
	global_load_lds_dwordx4 v[2:3], off
	s_waitcnt vmcnt(6)
	s_barrier
	s_setprio 1
	v_mfma_scale_f32_16x16x128_f8f6f4 v[92:95], v[26:33], v[192:199], 0, v1, v35 op_sel_hi:[0,0,0]
	v_mfma_scale_f32_16x16x128_f8f6f4 v[84:87], v[18:25], v[192:199], 0, v1, v35 op_sel_hi:[0,0,0]
	v_mfma_scale_f32_16x16x128_f8f6f4 v[76:79], v[26:33], v[200:207], 0, v1, v35 op_sel_hi:[0,0,0]
	v_mfma_scale_f32_16x16x128_f8f6f4 v[68:71], v[18:25], v[200:207], 0, v1, v35 op_sel_hi:[0,0,0]
	v_mfma_scale_f32_16x16x128_f8f6f4 v[60:63], v[26:33], v[218:225], 0, v1, v35 op_sel_hi:[0,0,0]
	v_mfma_scale_f32_16x16x128_f8f6f4 v[52:55], v[18:25], v[218:225], 0, v1, v35 op_sel_hi:[0,0,0]
	v_mfma_scale_f32_16x16x128_f8f6f4 v[44:47], v[26:33], v[226:233], 0, v1, v35 op_sel_hi:[0,0,0]
	v_mfma_scale_f32_16x16x128_f8f6f4 v[36:39], v[18:25], v[226:233], 0, v1, v35 op_sel_hi:[0,0,0]
	s_setprio 0
	s_add_i32 s79, 0, 0x18000
	v_add_u32_e32 v6, s79, v184
	s_barrier
	ds_read_b128 v[10:13], v6
	ds_read_b128 v[14:17], v6 offset:1024
	ds_read_b128 v[2:5], v6 offset:2048
	ds_read_b128 v[6:9], v6 offset:3072
	s_mov_b32 m0, s63
	ds_read_b128 v[18:21], v185 offset:32768
	ds_read_b128 v[22:25], v185 offset:33792
	ds_read_b128 v[26:29], v185 offset:34816
	ds_read_b128 v[30:33], v185 offset:35840
	ds_read_b128 v[192:195], v185 offset:36864
	ds_read_b128 v[196:199], v185 offset:37888
	ds_read_b128 v[200:203], v185 offset:38912
	ds_read_b128 v[204:207], v185 offset:39936
	s_nop 0
	global_load_lds_dwordx4 v210, s[48:49]
	s_mov_b32 m0, s64
	s_nop 0
	global_load_lds_dwordx4 v211, s[48:49]
	s_waitcnt lgkmcnt(8)
	s_barrier
	s_waitcnt lgkmcnt(0)
	s_setprio 1
	s_waitcnt lgkmcnt(0)
	v_mfma_scale_f32_16x16x128_f8f6f4 v[160:163], v[10:17], v[18:25], v[160:163], v176, v35 op_sel_hi:[0,0,0]
	v_mfma_scale_f32_16x16x128_f8f6f4 v[152:155], v[2:9], v[18:25], v[152:155], v176, v35 op_sel_hi:[0,0,0]
	v_mfma_scale_f32_16x16x128_f8f6f4 v[144:147], v[10:17], v[26:33], v[144:147], v176, v35 op_sel_hi:[0,0,0]
	v_mfma_scale_f32_16x16x128_f8f6f4 v[136:139], v[2:9], v[26:33], v[136:139], v176, v35 op_sel_hi:[0,0,0]
	v_mfma_scale_f32_16x16x128_f8f6f4 v[128:131], v[10:17], v[192:199], v[128:131], v176, v35 op_sel_hi:[0,0,0]
	v_mfma_scale_f32_16x16x128_f8f6f4 v[120:123], v[2:9], v[192:199], v[120:123], v176, v35 op_sel_hi:[0,0,0]
	v_mfma_scale_f32_16x16x128_f8f6f4 v[112:115], v[10:17], v[200:207], v[112:115], v176, v35 op_sel_hi:[0,0,0]
	v_mfma_scale_f32_16x16x128_f8f6f4 v[104:107], v[2:9], v[200:207], v[104:107], v176, v35 op_sel_hi:[0,0,0]
	s_setprio 0
	s_barrier
	s_add_i32 s80, 0, 0x1c000
	s_add_u32 s48, s42, 0x80
	v_add_u32_e32 v208, s80, v184
	s_addc_u32 s49, s43, 0
	s_add_i32 s79, s79, s58
	ds_read_b128 v[218:221], v208
	ds_read_b128 v[222:225], v208 offset:1024
	ds_read_b128 v[226:229], v208 offset:2048
	ds_read_b128 v[230:233], v208 offset:3072
	s_mov_b32 m0, s79
	v_lshl_add_u64 v[208:209], s[48:49], 0, v[164:165]
	global_load_lds_dwordx4 v[208:209], off
	v_lshl_add_u64 v[208:209], s[48:49], 0, v[166:167]
	s_add_i32 m0, s79, 0x2000
	s_nop 0
	global_load_lds_dwordx4 v[208:209], off
	s_barrier
	s_waitcnt lgkmcnt(0)
	s_setprio 1
	s_waitcnt lgkmcnt(0)
	v_mfma_scale_f32_16x16x128_f8f6f4 v[156:159], v[218:225], v[18:25], v[156:159], v1, v35 op_sel_hi:[0,0,0]
	v_mfma_scale_f32_16x16x128_f8f6f4 v[148:151], v[226:233], v[18:25], v[148:151], v1, v35 op_sel_hi:[0,0,0]
	v_mfma_scale_f32_16x16x128_f8f6f4 v[140:143], v[218:225], v[26:33], v[140:143], v1, v35 op_sel_hi:[0,0,0]
	v_mfma_scale_f32_16x16x128_f8f6f4 v[132:135], v[226:233], v[26:33], v[132:135], v1, v35 op_sel_hi:[0,0,0]
	v_mfma_scale_f32_16x16x128_f8f6f4 v[124:127], v[218:225], v[192:199], v[124:127], v1, v35 op_sel_hi:[0,0,0]
	v_mfma_scale_f32_16x16x128_f8f6f4 v[116:119], v[226:233], v[192:199], v[116:119], v1, v35 op_sel_hi:[0,0,0]
	v_mfma_scale_f32_16x16x128_f8f6f4 v[108:111], v[218:225], v[200:207], v[108:111], v1, v35 op_sel_hi:[0,0,0]
	v_mfma_scale_f32_16x16x128_f8f6f4 v[100:103], v[226:233], v[200:207], v[100:103], v1, v35 op_sel_hi:[0,0,0]
	s_setprio 0
	s_mov_b32 m0, s65
	s_barrier
	ds_read_b128 v[18:21], v185 offset:49152
	ds_read_b128 v[22:25], v185 offset:50176
	ds_read_b128 v[26:29], v185 offset:51200
	ds_read_b128 v[30:33], v185 offset:52224
	ds_read_b128 v[192:195], v185 offset:53248
	ds_read_b128 v[196:199], v185 offset:54272
	ds_read_b128 v[200:203], v185 offset:55296
	ds_read_b128 v[204:207], v185 offset:56320
	s_nop 0
	global_load_lds_dwordx4 v191, s[46:47]
	s_mov_b32 m0, s70
	s_nop 0
	global_load_lds_dwordx4 v190, s[46:47]
	s_barrier
	s_waitcnt lgkmcnt(0)
	s_setprio 1
	s_waitcnt lgkmcnt(0)
	v_mfma_scale_f32_16x16x128_f8f6f4 v[96:99], v[10:17], v[18:25], v[96:99], v176, v35 op_sel_hi:[0,0,0]
	v_mfma_scale_f32_16x16x128_f8f6f4 v[88:91], v[2:9], v[18:25], v[88:91], v176, v35 op_sel_hi:[0,0,0]
	v_mfma_scale_f32_16x16x128_f8f6f4 v[80:83], v[10:17], v[26:33], v[80:83], v176, v35 op_sel_hi:[0,0,0]
	v_mfma_scale_f32_16x16x128_f8f6f4 v[72:75], v[2:9], v[26:33], v[72:75], v176, v35 op_sel_hi:[0,0,0]
	v_mfma_scale_f32_16x16x128_f8f6f4 v[64:67], v[10:17], v[192:199], v[64:67], v176, v35 op_sel_hi:[0,0,0]
	v_mfma_scale_f32_16x16x128_f8f6f4 v[56:59], v[2:9], v[192:199], v[56:59], v176, v35 op_sel_hi:[0,0,0]
	v_mfma_scale_f32_16x16x128_f8f6f4 v[48:51], v[10:17], v[200:207], v[48:51], v176, v35 op_sel_hi:[0,0,0]
	v_mfma_scale_f32_16x16x128_f8f6f4 v[40:43], v[2:9], v[200:207], v[40:43], v176, v35 op_sel_hi:[0,0,0]
	s_setprio 0
	s_barrier
	s_add_u32 s42, s42, 0x20080
	s_addc_u32 s43, s43, 0
	s_add_i32 s46, s80, s58
	s_mov_b32 m0, s46
	v_lshl_add_u64 v[2:3], s[42:43], 0, v[164:165]
	global_load_lds_dwordx4 v[2:3], off
	v_lshl_add_u64 v[2:3], s[42:43], 0, v[166:167]
	s_add_i32 m0, s46, 0x2000
	s_nop 0
	global_load_lds_dwordx4 v[2:3], off
	s_waitcnt vmcnt(6)
	s_barrier
	s_setprio 1
	v_mfma_scale_f32_16x16x128_f8f6f4 v[92:95], v[218:225], v[18:25], v[92:95], v1, v35 op_sel_hi:[0,0,0]
	v_mfma_scale_f32_16x16x128_f8f6f4 v[84:87], v[226:233], v[18:25], v[84:87], v1, v35 op_sel_hi:[0,0,0]
	v_mfma_scale_f32_16x16x128_f8f6f4 v[76:79], v[218:225], v[26:33], v[76:79], v1, v35 op_sel_hi:[0,0,0]
	v_mfma_scale_f32_16x16x128_f8f6f4 v[68:71], v[226:233], v[26:33], v[68:71], v1, v35 op_sel_hi:[0,0,0]
	v_mfma_scale_f32_16x16x128_f8f6f4 v[60:63], v[218:225], v[192:199], v[60:63], v1, v35 op_sel_hi:[0,0,0]
	v_mfma_scale_f32_16x16x128_f8f6f4 v[52:55], v[226:233], v[192:199], v[52:55], v1, v35 op_sel_hi:[0,0,0]
	v_mfma_scale_f32_16x16x128_f8f6f4 v[44:47], v[218:225], v[200:207], v[44:47], v1, v35 op_sel_hi:[0,0,0]
	v_mfma_scale_f32_16x16x128_f8f6f4 v[36:39], v[226:233], v[200:207], v[36:39], v1, v35 op_sel_hi:[0,0,0]
	s_setprio 0
	s_add_i32 s1, s1, 2
	s_add_u32 s18, s18, 0x100
	s_addc_u32 s19, s19, 0
	s_cmp_gt_u32 s1, 5
	s_barrier
	s_cbranch_scc1 .LBB0_1239
	s_branch .LBB0_1248
